# v52: v34 + expert-weight f32->fp8 conversion rewritten so every fp8 store covers whole 128-byte lines (a wave converts 128 k x 32 n instead of 64 k x 64 n; register-staged, two half-items in flight);
# speedup vs baseline: 1.0274x; 1.0274x over previous
; #define LAS __attribute__((address_space(3)))
; __device__ __forceinline__ void moe_convert_queue(const Frame& F, const Args& A) {
;     unsigned char* ws = A.ws;
;     unsigned* Q = (unsigned*)(ws + WS_CTL) + CW_Q;
;     LAS int* qb = (LAS int*)(F.lds + LDSCTL_OFF + 1536);
;     LAS unsigned char* slice = F.lds + RING_OFF + F.wave * 16384;
;     for (;;) {
;         __syncthreads();
;         if (F.tid == 0) *qb = (int)__hip_atomic_fetch_add(Q, (unsigned)MQ_GRAB, __ATOMIC_RELAXED, __HIP_MEMORY_SCOPE_AGENT);
;         __syncthreads();
;         const int base = __builtin_amdgcn_readfirstlane(*qb);
;         if (base >= MQ_N) break;
; #pragma unroll 1
;         for (int k = 0; k < 2 * (MQ_GRAB / NWAVES); ++k) { const int r = base + F.wave * (MQ_GRAB / NWAVES) + (k >> 1), kh = k & 1;
.LBB0_262:
	s_add_u32 s4, s88, 0x20000
	s_addc_u32 s5, s89, 0
	v_readlane_b32 s6, v254, 32
	s_add_u32 s15, s88, 0x60e00000
	s_addc_u32 s16, s89, 0
	s_add_u32 s17, s88, 0x40e00000
	s_addc_u32 s18, s89, 0
	s_lshl_b32 s19, s6, 1
	s_mov_b32 s20, 0x20600
	s_mov_b32 s7, 0
	s_mov_b32 s22, 0x42800000
	s_mov_b32 s23, 0x42800000
	v_cmp_eq_u32_e64 s[2:3], 0, v0
	v_and_b32_e32 v1, 7, v0
	v_and_b32_e32 v4, 56, v0
	v_lshlrev_b32_e32 v4, 1, v4
	v_mov_b32_e32 v3, 0
	v_lshlrev_b32_e32 v2, 4, v1
	v_lshl_add_u32 v6, v1, 13, v4
	v_add_u32_e32 v9, 0x1000, v6
	v_mov_b32_e32 v7, s20
	v_mov_b32_e32 v98, 16
	s_and_saveexec_b64 s[8:9], s[2:3]
	s_cbranch_execz .Lcq_pf0
	global_atomic_add v96, v3, v98, s[4:5] sc0

; #define LAS __attribute__((address_space(3)))
; __device__ __forceinline__ void mq_half_dma(const float* W, int N, int k0, int n0, LAS unsigned char* slice, int lane) {
;     const float* src = W + (size_t)(k0 + (lane >> 4)) * N + n0 + 4 * (lane & 15);
; #pragma unroll
;     for (int j = 0; j < 16; ++j) __builtin_amdgcn_global_load_lds((const unsigned*)(src + (size_t)(4 * j) * N), (LAS unsigned*)(slice + j * 1024), 16, 0, 2);
; }
; __device__ __forceinline__ void moe_convert_queue(const Frame& F, const Args& A) {
;     ...
;         if (F.tid == 0) *qb = (int)__hip_atomic_fetch_add(Q, (unsigned)MQ_GRAB, __ATOMIC_RELAXED, __HIP_MEMORY_SCOPE_AGENT);
;         __syncthreads();
;         const int base = __builtin_amdgcn_readfirstlane(*qb);
;         if (base >= MQ_N) break;
; #pragma unroll 1
;         for (int k = 0; k < 2 * (MQ_GRAB / NWAVES); ++k) { const int r = base + F.wave * (MQ_GRAB / NWAVES) + (k >> 1), kh = k & 1;
;             const float* W; unsigned char* WT; int N, k0, n0, drow;
;             if (r < MQ_GU) { const int e = r / 1024, rr = r % 1024, kb = rr / 64, nb = rr % 64; const int pn = nb >> 2, q = nb & 3;
;                 W = A.in[I_WGU] + (size_t)e * 2048 * 4096; N = 4096; k0 = kb * 128 + 64 * kh; n0 = (q >> 1) * 2048 + 128 * pn + (q & 1) * 64; WT = (unsigned char*)(ws + WS_WGUT) + (size_t)e * 4096 * 2048; drow = nb * 64; }
;             else { const int r2 = r - MQ_GU, e = r2 / 512, rr = r2 % 512, kb = rr / 32, nb = rr % 32;
;                 W = A.in[I_WD] + (size_t)e * 2048 * 2048; N = 2048; k0 = kb * 128 + 64 * kh; n0 = nb * 64; WT = (unsigned char*)(ws + WS_WDT) + (size_t)e * 2048 * 2048; drow = nb * 64; }
;             asm volatile("s_waitcnt lgkmcnt(0)" ::: "memory");
;             mq_half_dma(W, N, k0, n0, slice, F.lane);
.Lcq_grab:
	s_waitcnt vmcnt(0)
	s_barrier
	s_and_saveexec_b64 s[8:9], s[2:3]
	s_cbranch_execz .Lcq_pf1
	v_mov_b32_e32 v97, v96
	ds_write_b32 v7, v97
	global_atomic_add v96, v3, v98, s[4:5] sc0
.Lcq_pf1:
	s_or_b64 exec, exec, s[8:9]
	s_waitcnt lgkmcnt(0)
	s_barrier
	ds_read_b32 v10, v7
	s_waitcnt lgkmcnt(0)
	v_readfirstlane_b32 s36, v10
	s_cmp_gt_i32 s36, 0xbfff
	s_cbranch_scc1 .Lcq_done
	s_add_i32 s36, s36, s19
	s_add_i32 s42, s36, 0
	s_cmpk_gt_i32 s42, 0x7fff
	s_cbranch_scc1 .Lcq_dn0
	s_lshr_b32 s6, s42, 10
	s_and_b32 s8, s42, 0x3ff
	s_lshr_b32 s9, s8, 6
	s_and_b32 s8, s8, 63
	s_lshl_b32 s38, s9, 7
	s_lshl_b32 s39, s8, 6
	s_lshr_b32 s9, s8, 2
	s_lshl_b32 s9, s9, 7
	s_and_b32 s12, s8, 1
	s_lshl_b32 s12, s12, 6
	s_add_i32 s12, s12, s9
	s_and_b32 s9, s8, 2
	s_lshl_b32 s9, s9, 10
	s_add_i32 s12, s12, s9
	s_lshl_b64 s[10:11], s[6:7], 25
	s_add_u32 s10, s76, s10
	s_addc_u32 s11, s77, s11
	s_lshl_b64 s[8:9], s[6:7], 23
	s_add_u32 s8, s17, s8
	s_addc_u32 s9, s18, s9
	s_movk_i32 s40, 0x1000
	s_branch .Lcq_ad0
.Lcq_dn0:
	s_add_i32 s8, s42, 0xffff8000
	s_lshr_b32 s6, s8, 9
	s_and_b32 s8, s8, 0x1ff
	s_lshr_b32 s9, s8, 5
	s_and_b32 s8, s8, 31
	s_lshl_b32 s38, s9, 7
	s_lshl_b32 s39, s8, 6
	s_mov_b32 s12, s39
	s_lshl_b64 s[10:11], s[6:7], 24
	s_add_u32 s10, s80, s10
	s_addc_u32 s11, s81, s11
	s_lshl_b64 s[8:9], s[6:7], 22
	s_add_u32 s8, s15, s8
	s_addc_u32 s9, s16, s9
	s_movk_i32 s40, 0x800
.Lcq_ad0:
	s_mul_i32 s13, s38, s40
	s_add_i32 s13, s13, s12
	s_lshl_b32 s13, s13, 2
	s_add_u32 s10, s10, s13
	s_addc_u32 s11, s11, 0
	s_lshl_b32 s41, s40, 2
	v_mad_u32_u24 v8, v4, s41, v2
	s_lshl_b32 s13, s39, 11
	s_add_i32 s13, s13, s38
	s_add_u32 s24, s8, s13
	s_addc_u32 s25, s9, 0
	global_load_dwordx4 v[10:13], v8, s[10:11] nt
	s_add_u32 s10, s10, s41
	s_addc_u32 s11, s11, 0
	global_load_dwordx4 v[14:17], v8, s[10:11] nt
	s_add_u32 s10, s10, s41
	s_addc_u32 s11, s11, 0
	global_load_dwordx4 v[18:21], v8, s[10:11] nt
	s_add_u32 s10, s10, s41
	s_addc_u32 s11, s11, 0
	global_load_dwordx4 v[22:25], v8, s[10:11] nt
	s_add_u32 s10, s10, s41
	s_addc_u32 s11, s11, 0
	global_load_dwordx4 v[26:29], v8, s[10:11] nt
	s_add_u32 s10, s10, s41
	s_addc_u32 s11, s11, 0
	global_load_dwordx4 v[30:33], v8, s[10:11] nt
	s_add_u32 s10, s10, s41
	s_addc_u32 s11, s11, 0
	global_load_dwordx4 v[34:37], v8, s[10:11] nt
	s_add_u32 s10, s10, s41
	s_addc_u32 s11, s11, 0
	global_load_dwordx4 v[38:41], v8, s[10:11] nt
	s_add_u32 s10, s10, s41
	s_addc_u32 s11, s11, 0
	global_load_dwordx4 v[42:45], v8, s[10:11] nt
	s_add_u32 s10, s10, s41
	s_addc_u32 s11, s11, 0
	global_load_dwordx4 v[46:49], v8, s[10:11] nt
	s_add_u32 s10, s10, s41
	s_addc_u32 s11, s11, 0
	global_load_dwordx4 v[50:53], v8, s[10:11] nt
	s_add_u32 s10, s10, s41
	s_addc_u32 s11, s11, 0
	global_load_dwordx4 v[54:57], v8, s[10:11] nt
	s_add_u32 s10, s10, s41
	s_addc_u32 s11, s11, 0
	global_load_dwordx4 v[58:61], v8, s[10:11] nt
	s_add_u32 s10, s10, s41
	s_addc_u32 s11, s11, 0
	global_load_dwordx4 v[62:65], v8, s[10:11] nt
	s_add_u32 s10, s10, s41
	s_addc_u32 s11, s11, 0
	global_load_dwordx4 v[66:69], v8, s[10:11] nt
	s_add_u32 s10, s10, s41
	s_addc_u32 s11, s11, 0
	global_load_dwordx4 v[70:73], v8, s[10:11] nt
	s_add_i32 s42, s36, 0
	s_cmpk_gt_i32 s42, 0x7fff
	s_cbranch_scc1 .Lcq_dn1
	s_lshr_b32 s6, s42, 10
	s_and_b32 s8, s42, 0x3ff
	s_lshr_b32 s9, s8, 6
	s_and_b32 s8, s8, 63
	s_lshl_b32 s38, s9, 7
	s_lshl_b32 s39, s8, 6
	s_lshr_b32 s9, s8, 2
	s_lshl_b32 s9, s9, 7
	s_and_b32 s12, s8, 1
	s_lshl_b32 s12, s12, 6
	s_add_i32 s12, s12, s9
	s_and_b32 s9, s8, 2
	s_lshl_b32 s9, s9, 10
	s_add_i32 s12, s12, s9
	s_add_i32 s12, s12, 32
	s_or_b32 s39, s39, 32
	s_lshl_b64 s[10:11], s[6:7], 25
	s_add_u32 s10, s76, s10
	s_addc_u32 s11, s77, s11
	s_lshl_b64 s[8:9], s[6:7], 23
	s_add_u32 s8, s17, s8
	s_addc_u32 s9, s18, s9
	s_movk_i32 s40, 0x1000
	s_branch .Lcq_ad1
.Lcq_dn1:
	s_add_i32 s8, s42, 0xffff8000
	s_lshr_b32 s6, s8, 9
	s_and_b32 s8, s8, 0x1ff
	s_lshr_b32 s9, s8, 5
	s_and_b32 s8, s8, 31
	s_lshl_b32 s38, s9, 7
	s_lshl_b32 s39, s8, 6
	s_or_b32 s39, s39, 32
	s_mov_b32 s12, s39
	s_lshl_b64 s[10:11], s[6:7], 24
	s_add_u32 s10, s80, s10
	s_addc_u32 s11, s81, s11
	s_lshl_b64 s[8:9], s[6:7], 22
	s_add_u32 s8, s15, s8
	s_addc_u32 s9, s16, s9
	s_movk_i32 s40, 0x800
; __device__ __forceinline__ unsigned pack_fp8x4(float a, float b, float c, float d) { int w = __builtin_amdgcn_cvt_pk_fp8_f32(a, b, 0, false); w = __builtin_amdgcn_cvt_pk_fp8_f32(c, d, w, true); return (unsigned)w; }
; #define LAS __attribute__((address_space(3)))
; __device__ __forceinline__ void mq_half_cvt(unsigned char* WT, int dst_row0, int k0, const LAS unsigned char* slice, int lane) {
;     const int kq = lane >> 4, nq = lane & 15;
;     f32x4 v[16];
; #pragma unroll
;     for (int i = 0; i < 16; ++i) v[i] = *(const LAS f32x4*)(slice + (16 * kq + i) * 256 + nq * 16);
; #pragma unroll
;     for (int i = 0; i < 4; ++i) { v4u o;
;         o.x = pg8::pack_fp8x4(v[0][i] * 64.f, v[1][i] * 64.f, v[2][i] * 64.f, v[3][i] * 64.f); o.y = pg8::pack_fp8x4(v[4][i] * 64.f, v[5][i] * 64.f, v[6][i] * 64.f, v[7][i] * 64.f);
;         o.z = pg8::pack_fp8x4(v[8][i] * 64.f, v[9][i] * 64.f, v[10][i] * 64.f, v[11][i] * 64.f); o.w = pg8::pack_fp8x4(v[12][i] * 64.f, v[13][i] * 64.f, v[14][i] * 64.f, v[15][i] * 64.f);
;         __builtin_nontemporal_store(o, (v4u*)(WT + (size_t)(dst_row0 + 4 * nq + i) * 2048 + k0 + 16 * kq)); }
; __device__ __forceinline__ void moe_convert_queue(const Frame& F, const Args& A) {
;     ...
;         for (int k = 0; k < 2 * (MQ_GRAB / NWAVES); ++k) { const int r = base + F.wave * (MQ_GRAB / NWAVES) + (k >> 1), kh = k & 1;
;             const float* W; unsigned char* WT; int N, k0, n0, drow;
;             if (r < MQ_GU) { const int e = r / 1024, rr = r % 1024, kb = rr / 64, nb = rr % 64; const int pn = nb >> 2, q = nb & 3;
;                 W = A.in[I_WGU] + (size_t)e * 2048 * 4096; N = 4096; k0 = kb * 128 + 64 * kh; n0 = (q >> 1) * 2048 + 128 * pn + (q & 1) * 64; WT = (unsigned char*)(ws + WS_WGUT) + (size_t)e * 4096 * 2048; drow = nb * 64; }
;             else { const int r2 = r - MQ_GU, e = r2 / 512, rr = r2 % 512, kb = rr / 32, nb = rr % 32;
;                 W = A.in[I_WD] + (size_t)e * 2048 * 2048; N = 2048; k0 = kb * 128 + 64 * kh; n0 = nb * 64; WT = (unsigned char*)(ws + WS_WDT) + (size_t)e * 2048 * 2048; drow = nb * 64; }
.Lcq_ad1:
	s_mul_i32 s13, s38, s40
	s_add_i32 s13, s13, s12
	s_lshl_b32 s13, s13, 2
	s_add_u32 s10, s10, s13
	s_addc_u32 s11, s11, 0
	s_lshl_b32 s41, s40, 2
	v_mad_u32_u24 v8, v4, s41, v2
	s_lshl_b32 s13, s39, 11
	s_add_i32 s13, s13, s38
	s_add_u32 s26, s8, s13
	s_addc_u32 s27, s9, 0
	global_load_dwordx4 v[100:103], v8, s[10:11] nt
	s_add_u32 s10, s10, s41
	s_addc_u32 s11, s11, 0
	global_load_dwordx4 v[104:107], v8, s[10:11] nt
	s_add_u32 s10, s10, s41
	s_addc_u32 s11, s11, 0
	global_load_dwordx4 v[108:111], v8, s[10:11] nt
	s_add_u32 s10, s10, s41
	s_addc_u32 s11, s11, 0
	global_load_dwordx4 v[112:115], v8, s[10:11] nt
	s_add_u32 s10, s10, s41
	s_addc_u32 s11, s11, 0
	global_load_dwordx4 v[116:119], v8, s[10:11] nt
	s_add_u32 s10, s10, s41
	s_addc_u32 s11, s11, 0
	global_load_dwordx4 v[120:123], v8, s[10:11] nt
	s_add_u32 s10, s10, s41
	s_addc_u32 s11, s11, 0
	global_load_dwordx4 v[124:127], v8, s[10:11] nt
	s_add_u32 s10, s10, s41
	s_addc_u32 s11, s11, 0
	global_load_dwordx4 v[128:131], v8, s[10:11] nt
	s_add_u32 s10, s10, s41
	s_addc_u32 s11, s11, 0
	global_load_dwordx4 v[132:135], v8, s[10:11] nt
	s_add_u32 s10, s10, s41
	s_addc_u32 s11, s11, 0
	global_load_dwordx4 v[136:139], v8, s[10:11] nt
	s_add_u32 s10, s10, s41
	s_addc_u32 s11, s11, 0
	global_load_dwordx4 v[140:143], v8, s[10:11] nt
	s_add_u32 s10, s10, s41
	s_addc_u32 s11, s11, 0
	global_load_dwordx4 v[144:147], v8, s[10:11] nt
	s_add_u32 s10, s10, s41
	s_addc_u32 s11, s11, 0
	global_load_dwordx4 v[148:151], v8, s[10:11] nt
	s_add_u32 s10, s10, s41
	s_addc_u32 s11, s11, 0
	global_load_dwordx4 v[152:155], v8, s[10:11] nt
	s_add_u32 s10, s10, s41
	s_addc_u32 s11, s11, 0
	global_load_dwordx4 v[156:159], v8, s[10:11] nt
	s_add_u32 s10, s10, s41
	s_addc_u32 s11, s11, 0
	global_load_dwordx4 v[160:163], v8, s[10:11] nt
	s_waitcnt vmcnt(16)
	v_pk_mul_f32 v[10:11], v[10:11], s[22:23] op_sel_hi:[1,0]
	v_pk_mul_f32 v[12:13], v[12:13], s[22:23] op_sel_hi:[1,0]
	v_pk_mul_f32 v[14:15], v[14:15], s[22:23] op_sel_hi:[1,0]
	v_pk_mul_f32 v[16:17], v[16:17], s[22:23] op_sel_hi:[1,0]
	v_pk_mul_f32 v[18:19], v[18:19], s[22:23] op_sel_hi:[1,0]
	v_pk_mul_f32 v[20:21], v[20:21], s[22:23] op_sel_hi:[1,0]
	v_pk_mul_f32 v[22:23], v[22:23], s[22:23] op_sel_hi:[1,0]
	v_pk_mul_f32 v[24:25], v[24:25], s[22:23] op_sel_hi:[1,0]
	v_pk_mul_f32 v[26:27], v[26:27], s[22:23] op_sel_hi:[1,0]
	v_pk_mul_f32 v[28:29], v[28:29], s[22:23] op_sel_hi:[1,0]
	v_pk_mul_f32 v[30:31], v[30:31], s[22:23] op_sel_hi:[1,0]
	v_pk_mul_f32 v[32:33], v[32:33], s[22:23] op_sel_hi:[1,0]
	v_pk_mul_f32 v[34:35], v[34:35], s[22:23] op_sel_hi:[1,0]
	v_pk_mul_f32 v[36:37], v[36:37], s[22:23] op_sel_hi:[1,0]
	v_pk_mul_f32 v[38:39], v[38:39], s[22:23] op_sel_hi:[1,0]
	v_pk_mul_f32 v[40:41], v[40:41], s[22:23] op_sel_hi:[1,0]
	v_pk_mul_f32 v[42:43], v[42:43], s[22:23] op_sel_hi:[1,0]
	v_pk_mul_f32 v[44:45], v[44:45], s[22:23] op_sel_hi:[1,0]
	v_pk_mul_f32 v[46:47], v[46:47], s[22:23] op_sel_hi:[1,0]
	v_pk_mul_f32 v[48:49], v[48:49], s[22:23] op_sel_hi:[1,0]
	v_pk_mul_f32 v[50:51], v[50:51], s[22:23] op_sel_hi:[1,0]
	v_pk_mul_f32 v[52:53], v[52:53], s[22:23] op_sel_hi:[1,0]
	v_pk_mul_f32 v[54:55], v[54:55], s[22:23] op_sel_hi:[1,0]
	v_pk_mul_f32 v[56:57], v[56:57], s[22:23] op_sel_hi:[1,0]
	v_pk_mul_f32 v[58:59], v[58:59], s[22:23] op_sel_hi:[1,0]
	v_pk_mul_f32 v[60:61], v[60:61], s[22:23] op_sel_hi:[1,0]
	v_pk_mul_f32 v[62:63], v[62:63], s[22:23] op_sel_hi:[1,0]
	v_pk_mul_f32 v[64:65], v[64:65], s[22:23] op_sel_hi:[1,0]
	v_pk_mul_f32 v[66:67], v[66:67], s[22:23] op_sel_hi:[1,0]
	v_pk_mul_f32 v[68:69], v[68:69], s[22:23] op_sel_hi:[1,0]
	v_pk_mul_f32 v[70:71], v[70:71], s[22:23] op_sel_hi:[1,0]
	v_pk_mul_f32 v[72:73], v[72:73], s[22:23] op_sel_hi:[1,0]
	v_cvt_pk_fp8_f32 v74, v10, v14
	v_cvt_pk_fp8_f32 v75, v26, v30
	v_cvt_pk_fp8_f32 v76, v42, v46
	v_cvt_pk_fp8_f32 v77, v58, v62
	v_cvt_pk_fp8_f32 v74, v18, v22 op_sel:[0,0,1]
	v_cvt_pk_fp8_f32 v75, v34, v38 op_sel:[0,0,1]
	v_cvt_pk_fp8_f32 v76, v50, v54 op_sel:[0,0,1]
	v_cvt_pk_fp8_f32 v77, v66, v70 op_sel:[0,0,1]
	v_cvt_pk_fp8_f32 v84, v11, v15
	v_cvt_pk_fp8_f32 v85, v27, v31
	v_cvt_pk_fp8_f32 v86, v43, v47
	v_cvt_pk_fp8_f32 v87, v59, v63
	v_cvt_pk_fp8_f32 v84, v19, v23 op_sel:[0,0,1]
	v_cvt_pk_fp8_f32 v85, v35, v39 op_sel:[0,0,1]
	v_cvt_pk_fp8_f32 v86, v51, v55 op_sel:[0,0,1]
	v_cvt_pk_fp8_f32 v87, v67, v71 op_sel:[0,0,1]
	global_store_dwordx4 v6, v[74:77], s[24:25] nt
	v_cvt_pk_fp8_f32 v88, v12, v16
	v_cvt_pk_fp8_f32 v89, v28, v32
	v_cvt_pk_fp8_f32 v90, v44, v48
	v_cvt_pk_fp8_f32 v91, v60, v64
	v_cvt_pk_fp8_f32 v88, v20, v24 op_sel:[0,0,1]
	v_cvt_pk_fp8_f32 v89, v36, v40 op_sel:[0,0,1]
	v_cvt_pk_fp8_f32 v90, v52, v56 op_sel:[0,0,1]
	v_cvt_pk_fp8_f32 v91, v68, v72 op_sel:[0,0,1]
	global_store_dwordx4 v6, v[84:87], s[24:25] offset:2048 nt
	v_cvt_pk_fp8_f32 v92, v13, v17
	v_cvt_pk_fp8_f32 v93, v29, v33
	v_cvt_pk_fp8_f32 v94, v45, v49
	v_cvt_pk_fp8_f32 v95, v61, v65
	v_cvt_pk_fp8_f32 v92, v21, v25 op_sel:[0,0,1]
	v_cvt_pk_fp8_f32 v93, v37, v41 op_sel:[0,0,1]
	v_cvt_pk_fp8_f32 v94, v53, v57 op_sel:[0,0,1]
	v_cvt_pk_fp8_f32 v95, v69, v73 op_sel:[0,0,1]
	global_store_dwordx4 v9, v[88:91], s[24:25] nt
	s_nop 1
	global_store_dwordx4 v9, v[92:95], s[24:25] offset:2048 nt
	s_add_i32 s42, s36, 1
	s_cmpk_gt_i32 s42, 0x7fff
	s_cbranch_scc1 .Lcq_dn2
	s_lshr_b32 s6, s42, 10
	s_and_b32 s8, s42, 0x3ff
	s_lshr_b32 s9, s8, 6
	s_and_b32 s8, s8, 63
	s_lshl_b32 s38, s9, 7
	s_lshl_b32 s39, s8, 6
	s_lshr_b32 s9, s8, 2
	s_lshl_b32 s9, s9, 7
	s_and_b32 s12, s8, 1
	s_lshl_b32 s12, s12, 6
	s_add_i32 s12, s12, s9
	s_and_b32 s9, s8, 2
	s_lshl_b32 s9, s9, 10
	s_add_i32 s12, s12, s9
	s_lshl_b64 s[10:11], s[6:7], 25
	s_add_u32 s10, s76, s10
	s_addc_u32 s11, s77, s11
	s_lshl_b64 s[8:9], s[6:7], 23
	s_add_u32 s8, s17, s8
	s_addc_u32 s9, s18, s9
	s_movk_i32 s40, 0x1000
	s_branch .Lcq_ad2

; __device__ __forceinline__ unsigned pack_fp8x4(float a, float b, float c, float d) { int w = __builtin_amdgcn_cvt_pk_fp8_f32(a, b, 0, false); w = __builtin_amdgcn_cvt_pk_fp8_f32(c, d, w, true); return (unsigned)w; }
; #define LAS __attribute__((address_space(3)))
; __device__ __forceinline__ void mq_half_dma(const float* W, int N, int k0, int n0, LAS unsigned char* slice, int lane) {
;     const float* src = W + (size_t)(k0 + (lane >> 4)) * N + n0 + 4 * (lane & 15);
; #pragma unroll
;     for (int j = 0; j < 16; ++j) __builtin_amdgcn_global_load_lds((const unsigned*)(src + (size_t)(4 * j) * N), (LAS unsigned*)(slice + j * 1024), 16, 0, 2);
; }
; __device__ __forceinline__ void mq_half_cvt(unsigned char* WT, int dst_row0, int k0, const LAS unsigned char* slice, int lane) {
;     const int kq = lane >> 4, nq = lane & 15;
;     f32x4 v[16];
; #pragma unroll
;     for (int i = 0; i < 16; ++i) v[i] = *(const LAS f32x4*)(slice + (16 * kq + i) * 256 + nq * 16);
; #pragma unroll
;     for (int i = 0; i < 4; ++i) { v4u o;
;         o.x = pg8::pack_fp8x4(v[0][i] * 64.f, v[1][i] * 64.f, v[2][i] * 64.f, v[3][i] * 64.f); o.y = pg8::pack_fp8x4(v[4][i] * 64.f, v[5][i] * 64.f, v[6][i] * 64.f, v[7][i] * 64.f);
;         o.z = pg8::pack_fp8x4(v[8][i] * 64.f, v[9][i] * 64.f, v[10][i] * 64.f, v[11][i] * 64.f); o.w = pg8::pack_fp8x4(v[12][i] * 64.f, v[13][i] * 64.f, v[14][i] * 64.f, v[15][i] * 64.f);
;         __builtin_nontemporal_store(o, (v4u*)(WT + (size_t)(dst_row0 + 4 * nq + i) * 2048 + k0 + 16 * kq)); }
; __device__ __forceinline__ void moe_convert_queue(const Frame& F, const Args& A) {
;     ...
;             if (r < MQ_GU) { const int e = r / 1024, rr = r % 1024, kb = rr / 64, nb = rr % 64; const int pn = nb >> 2, q = nb & 3;
;                 W = A.in[I_WGU] + (size_t)e * 2048 * 4096; N = 4096; k0 = kb * 128 + 64 * kh; n0 = (q >> 1) * 2048 + 128 * pn + (q & 1) * 64; WT = (unsigned char*)(ws + WS_WGUT) + (size_t)e * 4096 * 2048; drow = nb * 64; }
.Lcq_ad2:
	s_mul_i32 s13, s38, s40
	s_add_i32 s13, s13, s12
	s_lshl_b32 s13, s13, 2
	s_add_u32 s10, s10, s13
	s_addc_u32 s11, s11, 0
	s_lshl_b32 s41, s40, 2
	v_mad_u32_u24 v8, v4, s41, v2
	s_lshl_b32 s13, s39, 11
	s_add_i32 s13, s13, s38
	s_add_u32 s24, s8, s13
	s_addc_u32 s25, s9, 0
	global_load_dwordx4 v[10:13], v8, s[10:11] nt
	s_add_u32 s10, s10, s41
	s_addc_u32 s11, s11, 0
	global_load_dwordx4 v[14:17], v8, s[10:11] nt
	s_add_u32 s10, s10, s41
	s_addc_u32 s11, s11, 0
	global_load_dwordx4 v[18:21], v8, s[10:11] nt
	s_add_u32 s10, s10, s41
	s_addc_u32 s11, s11, 0
	global_load_dwordx4 v[22:25], v8, s[10:11] nt
	s_add_u32 s10, s10, s41
	s_addc_u32 s11, s11, 0
	global_load_dwordx4 v[26:29], v8, s[10:11] nt
	s_add_u32 s10, s10, s41
	s_addc_u32 s11, s11, 0
	global_load_dwordx4 v[30:33], v8, s[10:11] nt
	s_add_u32 s10, s10, s41
	s_addc_u32 s11, s11, 0
	global_load_dwordx4 v[34:37], v8, s[10:11] nt
	s_add_u32 s10, s10, s41
	s_addc_u32 s11, s11, 0
	global_load_dwordx4 v[38:41], v8, s[10:11] nt
	s_add_u32 s10, s10, s41
	s_addc_u32 s11, s11, 0
	global_load_dwordx4 v[42:45], v8, s[10:11] nt
	s_add_u32 s10, s10, s41
	s_addc_u32 s11, s11, 0
	global_load_dwordx4 v[46:49], v8, s[10:11] nt
	s_add_u32 s10, s10, s41
	s_addc_u32 s11, s11, 0
	global_load_dwordx4 v[50:53], v8, s[10:11] nt
	s_add_u32 s10, s10, s41
	s_addc_u32 s11, s11, 0
	global_load_dwordx4 v[54:57], v8, s[10:11] nt
	s_add_u32 s10, s10, s41
	s_addc_u32 s11, s11, 0
	global_load_dwordx4 v[58:61], v8, s[10:11] nt
	s_add_u32 s10, s10, s41
	s_addc_u32 s11, s11, 0
	global_load_dwordx4 v[62:65], v8, s[10:11] nt
	s_add_u32 s10, s10, s41
	s_addc_u32 s11, s11, 0
	global_load_dwordx4 v[66:69], v8, s[10:11] nt
	s_add_u32 s10, s10, s41
	s_addc_u32 s11, s11, 0
	global_load_dwordx4 v[70:73], v8, s[10:11] nt
	s_waitcnt vmcnt(20)
	v_pk_mul_f32 v[100:101], v[100:101], s[22:23] op_sel_hi:[1,0]
	v_pk_mul_f32 v[102:103], v[102:103], s[22:23] op_sel_hi:[1,0]
	v_pk_mul_f32 v[104:105], v[104:105], s[22:23] op_sel_hi:[1,0]
	v_pk_mul_f32 v[106:107], v[106:107], s[22:23] op_sel_hi:[1,0]
	v_pk_mul_f32 v[108:109], v[108:109], s[22:23] op_sel_hi:[1,0]
	v_pk_mul_f32 v[110:111], v[110:111], s[22:23] op_sel_hi:[1,0]
	v_pk_mul_f32 v[112:113], v[112:113], s[22:23] op_sel_hi:[1,0]
	v_pk_mul_f32 v[114:115], v[114:115], s[22:23] op_sel_hi:[1,0]
	v_pk_mul_f32 v[116:117], v[116:117], s[22:23] op_sel_hi:[1,0]
	v_pk_mul_f32 v[118:119], v[118:119], s[22:23] op_sel_hi:[1,0]
	v_pk_mul_f32 v[120:121], v[120:121], s[22:23] op_sel_hi:[1,0]
	v_pk_mul_f32 v[122:123], v[122:123], s[22:23] op_sel_hi:[1,0]
	v_pk_mul_f32 v[124:125], v[124:125], s[22:23] op_sel_hi:[1,0]
	v_pk_mul_f32 v[126:127], v[126:127], s[22:23] op_sel_hi:[1,0]
	v_pk_mul_f32 v[128:129], v[128:129], s[22:23] op_sel_hi:[1,0]
	v_pk_mul_f32 v[130:131], v[130:131], s[22:23] op_sel_hi:[1,0]
	v_pk_mul_f32 v[132:133], v[132:133], s[22:23] op_sel_hi:[1,0]
	v_pk_mul_f32 v[134:135], v[134:135], s[22:23] op_sel_hi:[1,0]
	v_pk_mul_f32 v[136:137], v[136:137], s[22:23] op_sel_hi:[1,0]
	v_pk_mul_f32 v[138:139], v[138:139], s[22:23] op_sel_hi:[1,0]
	v_pk_mul_f32 v[140:141], v[140:141], s[22:23] op_sel_hi:[1,0]
	v_pk_mul_f32 v[142:143], v[142:143], s[22:23] op_sel_hi:[1,0]
	v_pk_mul_f32 v[144:145], v[144:145], s[22:23] op_sel_hi:[1,0]
	v_pk_mul_f32 v[146:147], v[146:147], s[22:23] op_sel_hi:[1,0]
	v_pk_mul_f32 v[148:149], v[148:149], s[22:23] op_sel_hi:[1,0]
	v_pk_mul_f32 v[150:151], v[150:151], s[22:23] op_sel_hi:[1,0]
	v_pk_mul_f32 v[152:153], v[152:153], s[22:23] op_sel_hi:[1,0]
	v_pk_mul_f32 v[154:155], v[154:155], s[22:23] op_sel_hi:[1,0]
	v_pk_mul_f32 v[156:157], v[156:157], s[22:23] op_sel_hi:[1,0]
	v_pk_mul_f32 v[158:159], v[158:159], s[22:23] op_sel_hi:[1,0]
	v_pk_mul_f32 v[160:161], v[160:161], s[22:23] op_sel_hi:[1,0]
	v_pk_mul_f32 v[162:163], v[162:163], s[22:23] op_sel_hi:[1,0]
	v_cvt_pk_fp8_f32 v74, v100, v104
	v_cvt_pk_fp8_f32 v75, v116, v120
	v_cvt_pk_fp8_f32 v76, v132, v136
	v_cvt_pk_fp8_f32 v77, v148, v152
	v_cvt_pk_fp8_f32 v74, v108, v112 op_sel:[0,0,1]
	v_cvt_pk_fp8_f32 v75, v124, v128 op_sel:[0,0,1]
	v_cvt_pk_fp8_f32 v76, v140, v144 op_sel:[0,0,1]
	v_cvt_pk_fp8_f32 v77, v156, v160 op_sel:[0,0,1]
	v_cvt_pk_fp8_f32 v84, v101, v105
	v_cvt_pk_fp8_f32 v85, v117, v121
	v_cvt_pk_fp8_f32 v86, v133, v137
	v_cvt_pk_fp8_f32 v87, v149, v153
	v_cvt_pk_fp8_f32 v84, v109, v113 op_sel:[0,0,1]
	v_cvt_pk_fp8_f32 v85, v125, v129 op_sel:[0,0,1]
	v_cvt_pk_fp8_f32 v86, v141, v145 op_sel:[0,0,1]
	v_cvt_pk_fp8_f32 v87, v157, v161 op_sel:[0,0,1]
	global_store_dwordx4 v6, v[74:77], s[26:27] nt
	v_cvt_pk_fp8_f32 v88, v102, v106
	v_cvt_pk_fp8_f32 v89, v118, v122
	v_cvt_pk_fp8_f32 v90, v134, v138
	v_cvt_pk_fp8_f32 v91, v150, v154
	v_cvt_pk_fp8_f32 v88, v110, v114 op_sel:[0,0,1]
	v_cvt_pk_fp8_f32 v89, v126, v130 op_sel:[0,0,1]
	v_cvt_pk_fp8_f32 v90, v142, v146 op_sel:[0,0,1]
	v_cvt_pk_fp8_f32 v91, v158, v162 op_sel:[0,0,1]
	global_store_dwordx4 v6, v[84:87], s[26:27] offset:2048 nt
	v_cvt_pk_fp8_f32 v92, v103, v107
	v_cvt_pk_fp8_f32 v93, v119, v123
	v_cvt_pk_fp8_f32 v94, v135, v139
	v_cvt_pk_fp8_f32 v95, v151, v155
	v_cvt_pk_fp8_f32 v92, v111, v115 op_sel:[0,0,1]
	v_cvt_pk_fp8_f32 v93, v127, v131 op_sel:[0,0,1]
	v_cvt_pk_fp8_f32 v94, v143, v147 op_sel:[0,0,1]
	v_cvt_pk_fp8_f32 v95, v159, v163 op_sel:[0,0,1]
	global_store_dwordx4 v9, v[88:91], s[26:27] nt
	s_nop 1
	global_store_dwordx4 v9, v[92:95], s[26:27] offset:2048 nt
	s_add_i32 s42, s36, 1
	s_cmpk_gt_i32 s42, 0x7fff
	s_cbranch_scc1 .Lcq_dn3
	s_lshr_b32 s6, s42, 10
	s_and_b32 s8, s42, 0x3ff
	s_lshr_b32 s9, s8, 6
	s_and_b32 s8, s8, 63
	s_lshl_b32 s38, s9, 7
	s_lshl_b32 s39, s8, 6
	s_lshr_b32 s9, s8, 2
	s_lshl_b32 s9, s9, 7
	s_and_b32 s12, s8, 1
	s_lshl_b32 s12, s12, 6
	s_add_i32 s12, s12, s9
	s_and_b32 s9, s8, 2
	s_lshl_b32 s9, s9, 10
	s_add_i32 s12, s12, s9
	s_add_i32 s12, s12, 32
	s_or_b32 s39, s39, 32
	s_lshl_b64 s[10:11], s[6:7], 25
	s_add_u32 s10, s76, s10
	s_addc_u32 s11, s77, s11
	s_lshl_b64 s[8:9], s[6:7], 23
	s_add_u32 s8, s17, s8
	s_addc_u32 s9, s18, s9
	s_movk_i32 s40, 0x1000
	s_branch .Lcq_ad3

; __device__ __forceinline__ unsigned pack_fp8x4(float a, float b, float c, float d) { int w = __builtin_amdgcn_cvt_pk_fp8_f32(a, b, 0, false); w = __builtin_amdgcn_cvt_pk_fp8_f32(c, d, w, true); return (unsigned)w; }
; #define LAS __attribute__((address_space(3)))
; __device__ __forceinline__ void mq_half_dma(const float* W, int N, int k0, int n0, LAS unsigned char* slice, int lane) {
;     const float* src = W + (size_t)(k0 + (lane >> 4)) * N + n0 + 4 * (lane & 15);
; #pragma unroll
;     for (int j = 0; j < 16; ++j) __builtin_amdgcn_global_load_lds((const unsigned*)(src + (size_t)(4 * j) * N), (LAS unsigned*)(slice + j * 1024), 16, 0, 2);
; }
; __device__ __forceinline__ void mq_half_cvt(unsigned char* WT, int dst_row0, int k0, const LAS unsigned char* slice, int lane) {
;     const int kq = lane >> 4, nq = lane & 15;
;     f32x4 v[16];
; #pragma unroll
;     for (int i = 0; i < 16; ++i) v[i] = *(const LAS f32x4*)(slice + (16 * kq + i) * 256 + nq * 16);
; #pragma unroll
;     for (int i = 0; i < 4; ++i) { v4u o;
;         o.x = pg8::pack_fp8x4(v[0][i] * 64.f, v[1][i] * 64.f, v[2][i] * 64.f, v[3][i] * 64.f); o.y = pg8::pack_fp8x4(v[4][i] * 64.f, v[5][i] * 64.f, v[6][i] * 64.f, v[7][i] * 64.f);
;         o.z = pg8::pack_fp8x4(v[8][i] * 64.f, v[9][i] * 64.f, v[10][i] * 64.f, v[11][i] * 64.f); o.w = pg8::pack_fp8x4(v[12][i] * 64.f, v[13][i] * 64.f, v[14][i] * 64.f, v[15][i] * 64.f);
;         __builtin_nontemporal_store(o, (v4u*)(WT + (size_t)(dst_row0 + 4 * nq + i) * 2048 + k0 + 16 * kq)); }
.Lcq_ad3:
	s_mul_i32 s13, s38, s40
	s_add_i32 s13, s13, s12
	s_lshl_b32 s13, s13, 2
	s_add_u32 s10, s10, s13
	s_addc_u32 s11, s11, 0
	s_lshl_b32 s41, s40, 2
	v_mad_u32_u24 v8, v4, s41, v2
	s_lshl_b32 s13, s39, 11
	s_add_i32 s13, s13, s38
	s_add_u32 s26, s8, s13
	s_addc_u32 s27, s9, 0
	global_load_dwordx4 v[100:103], v8, s[10:11] nt
	s_add_u32 s10, s10, s41
	s_addc_u32 s11, s11, 0
	global_load_dwordx4 v[104:107], v8, s[10:11] nt
	s_add_u32 s10, s10, s41
	s_addc_u32 s11, s11, 0
	global_load_dwordx4 v[108:111], v8, s[10:11] nt
	s_add_u32 s10, s10, s41
	s_addc_u32 s11, s11, 0
	global_load_dwordx4 v[112:115], v8, s[10:11] nt
	s_add_u32 s10, s10, s41
	s_addc_u32 s11, s11, 0
	global_load_dwordx4 v[116:119], v8, s[10:11] nt
	s_add_u32 s10, s10, s41
	s_addc_u32 s11, s11, 0
	global_load_dwordx4 v[120:123], v8, s[10:11] nt
	s_add_u32 s10, s10, s41
	s_addc_u32 s11, s11, 0
	global_load_dwordx4 v[124:127], v8, s[10:11] nt
	s_add_u32 s10, s10, s41
	s_addc_u32 s11, s11, 0
	global_load_dwordx4 v[128:131], v8, s[10:11] nt
	s_add_u32 s10, s10, s41
	s_addc_u32 s11, s11, 0
	global_load_dwordx4 v[132:135], v8, s[10:11] nt
	s_add_u32 s10, s10, s41
	s_addc_u32 s11, s11, 0
	global_load_dwordx4 v[136:139], v8, s[10:11] nt
	s_add_u32 s10, s10, s41
	s_addc_u32 s11, s11, 0
	global_load_dwordx4 v[140:143], v8, s[10:11] nt
	s_add_u32 s10, s10, s41
	s_addc_u32 s11, s11, 0
	global_load_dwordx4 v[144:147], v8, s[10:11] nt
	s_add_u32 s10, s10, s41
	s_addc_u32 s11, s11, 0
	global_load_dwordx4 v[148:151], v8, s[10:11] nt
	s_add_u32 s10, s10, s41
	s_addc_u32 s11, s11, 0
	global_load_dwordx4 v[152:155], v8, s[10:11] nt
	s_add_u32 s10, s10, s41
	s_addc_u32 s11, s11, 0
	global_load_dwordx4 v[156:159], v8, s[10:11] nt
	s_add_u32 s10, s10, s41
	s_addc_u32 s11, s11, 0
	global_load_dwordx4 v[160:163], v8, s[10:11] nt
	s_waitcnt vmcnt(20)
	v_pk_mul_f32 v[10:11], v[10:11], s[22:23] op_sel_hi:[1,0]
	v_pk_mul_f32 v[12:13], v[12:13], s[22:23] op_sel_hi:[1,0]
	v_pk_mul_f32 v[14:15], v[14:15], s[22:23] op_sel_hi:[1,0]
	v_pk_mul_f32 v[16:17], v[16:17], s[22:23] op_sel_hi:[1,0]
	v_pk_mul_f32 v[18:19], v[18:19], s[22:23] op_sel_hi:[1,0]
	v_pk_mul_f32 v[20:21], v[20:21], s[22:23] op_sel_hi:[1,0]
	v_pk_mul_f32 v[22:23], v[22:23], s[22:23] op_sel_hi:[1,0]
	v_pk_mul_f32 v[24:25], v[24:25], s[22:23] op_sel_hi:[1,0]
	v_pk_mul_f32 v[26:27], v[26:27], s[22:23] op_sel_hi:[1,0]
	v_pk_mul_f32 v[28:29], v[28:29], s[22:23] op_sel_hi:[1,0]
	v_pk_mul_f32 v[30:31], v[30:31], s[22:23] op_sel_hi:[1,0]
	v_pk_mul_f32 v[32:33], v[32:33], s[22:23] op_sel_hi:[1,0]
	v_pk_mul_f32 v[34:35], v[34:35], s[22:23] op_sel_hi:[1,0]
	v_pk_mul_f32 v[36:37], v[36:37], s[22:23] op_sel_hi:[1,0]
	v_pk_mul_f32 v[38:39], v[38:39], s[22:23] op_sel_hi:[1,0]
	v_pk_mul_f32 v[40:41], v[40:41], s[22:23] op_sel_hi:[1,0]
	v_pk_mul_f32 v[42:43], v[42:43], s[22:23] op_sel_hi:[1,0]
	v_pk_mul_f32 v[44:45], v[44:45], s[22:23] op_sel_hi:[1,0]
	v_pk_mul_f32 v[46:47], v[46:47], s[22:23] op_sel_hi:[1,0]
	v_pk_mul_f32 v[48:49], v[48:49], s[22:23] op_sel_hi:[1,0]
	v_pk_mul_f32 v[50:51], v[50:51], s[22:23] op_sel_hi:[1,0]
	v_pk_mul_f32 v[52:53], v[52:53], s[22:23] op_sel_hi:[1,0]
	v_pk_mul_f32 v[54:55], v[54:55], s[22:23] op_sel_hi:[1,0]
	v_pk_mul_f32 v[56:57], v[56:57], s[22:23] op_sel_hi:[1,0]
	v_pk_mul_f32 v[58:59], v[58:59], s[22:23] op_sel_hi:[1,0]
	v_pk_mul_f32 v[60:61], v[60:61], s[22:23] op_sel_hi:[1,0]
	v_pk_mul_f32 v[62:63], v[62:63], s[22:23] op_sel_hi:[1,0]
	v_pk_mul_f32 v[64:65], v[64:65], s[22:23] op_sel_hi:[1,0]
	v_pk_mul_f32 v[66:67], v[66:67], s[22:23] op_sel_hi:[1,0]
	v_pk_mul_f32 v[68:69], v[68:69], s[22:23] op_sel_hi:[1,0]
	v_pk_mul_f32 v[70:71], v[70:71], s[22:23] op_sel_hi:[1,0]
	v_pk_mul_f32 v[72:73], v[72:73], s[22:23] op_sel_hi:[1,0]
	v_cvt_pk_fp8_f32 v74, v10, v14
	v_cvt_pk_fp8_f32 v75, v26, v30
	v_cvt_pk_fp8_f32 v76, v42, v46
	v_cvt_pk_fp8_f32 v77, v58, v62
	v_cvt_pk_fp8_f32 v74, v18, v22 op_sel:[0,0,1]
	v_cvt_pk_fp8_f32 v75, v34, v38 op_sel:[0,0,1]
	v_cvt_pk_fp8_f32 v76, v50, v54 op_sel:[0,0,1]
	v_cvt_pk_fp8_f32 v77, v66, v70 op_sel:[0,0,1]
	v_cvt_pk_fp8_f32 v84, v11, v15
	v_cvt_pk_fp8_f32 v85, v27, v31
	v_cvt_pk_fp8_f32 v86, v43, v47
	v_cvt_pk_fp8_f32 v87, v59, v63
	v_cvt_pk_fp8_f32 v84, v19, v23 op_sel:[0,0,1]
	v_cvt_pk_fp8_f32 v85, v35, v39 op_sel:[0,0,1]
	v_cvt_pk_fp8_f32 v86, v51, v55 op_sel:[0,0,1]
	v_cvt_pk_fp8_f32 v87, v67, v71 op_sel:[0,0,1]
	global_store_dwordx4 v6, v[74:77], s[24:25] nt
	v_cvt_pk_fp8_f32 v88, v12, v16
	v_cvt_pk_fp8_f32 v89, v28, v32
	v_cvt_pk_fp8_f32 v90, v44, v48
	v_cvt_pk_fp8_f32 v91, v60, v64
	v_cvt_pk_fp8_f32 v88, v20, v24 op_sel:[0,0,1]
	v_cvt_pk_fp8_f32 v89, v36, v40 op_sel:[0,0,1]
	v_cvt_pk_fp8_f32 v90, v52, v56 op_sel:[0,0,1]
	v_cvt_pk_fp8_f32 v91, v68, v72 op_sel:[0,0,1]
	global_store_dwordx4 v6, v[84:87], s[24:25] offset:2048 nt
	v_cvt_pk_fp8_f32 v92, v13, v17
	v_cvt_pk_fp8_f32 v93, v29, v33
	v_cvt_pk_fp8_f32 v94, v45, v49
	v_cvt_pk_fp8_f32 v95, v61, v65
	v_cvt_pk_fp8_f32 v92, v21, v25 op_sel:[0,0,1]
	v_cvt_pk_fp8_f32 v93, v37, v41 op_sel:[0,0,1]
	v_cvt_pk_fp8_f32 v94, v53, v57 op_sel:[0,0,1]
	v_cvt_pk_fp8_f32 v95, v69, v73 op_sel:[0,0,1]
	global_store_dwordx4 v9, v[88:91], s[24:25] nt
	s_nop 1
	global_store_dwordx4 v9, v[92:95], s[24:25] offset:2048 nt
	s_waitcnt vmcnt(4)
; __device__ __forceinline__ unsigned pack_fp8x4(float a, float b, float c, float d) { int w = __builtin_amdgcn_cvt_pk_fp8_f32(a, b, 0, false); w = __builtin_amdgcn_cvt_pk_fp8_f32(c, d, w, true); return (unsigned)w; }
; __device__ __forceinline__ void xcd_barrier(const XcdBarrier& b) {
;     asm volatile("s_waitcnt vmcnt(0)" ::: "memory");
;     __syncthreads();
;     if (threadIdx.x == 0) {
;         unsigned* bar = b.bar;
;         __builtin_amdgcn_s_waitcnt(0);
;         unsigned nloc = b.st[0], nx = b.st[1];
;         if (nloc == 0u) { xcd_barrier_complete(bar, b.x, nloc, nx); b.st[0] = nloc; b.st[1] = nx; }
; __device__ __forceinline__ void mq_half_cvt(unsigned char* WT, int dst_row0, int k0, const LAS unsigned char* slice, int lane) {
;     ...
;     for (int i = 0; i < 4; ++i) { v4u o;
;         o.x = pg8::pack_fp8x4(v[0][i] * 64.f, v[1][i] * 64.f, v[2][i] * 64.f, v[3][i] * 64.f); o.y = pg8::pack_fp8x4(v[4][i] * 64.f, v[5][i] * 64.f, v[6][i] * 64.f, v[7][i] * 64.f);
;         o.z = pg8::pack_fp8x4(v[8][i] * 64.f, v[9][i] * 64.f, v[10][i] * 64.f, v[11][i] * 64.f); o.w = pg8::pack_fp8x4(v[12][i] * 64.f, v[13][i] * 64.f, v[14][i] * 64.f, v[15][i] * 64.f);
;         __builtin_nontemporal_store(o, (v4u*)(WT + (size_t)(dst_row0 + 4 * nq + i) * 2048 + k0 + 16 * kq)); }
	v_pk_mul_f32 v[100:101], v[100:101], s[22:23] op_sel_hi:[1,0]
	v_pk_mul_f32 v[102:103], v[102:103], s[22:23] op_sel_hi:[1,0]
	v_pk_mul_f32 v[104:105], v[104:105], s[22:23] op_sel_hi:[1,0]
	v_pk_mul_f32 v[106:107], v[106:107], s[22:23] op_sel_hi:[1,0]
	v_pk_mul_f32 v[108:109], v[108:109], s[22:23] op_sel_hi:[1,0]
	v_pk_mul_f32 v[110:111], v[110:111], s[22:23] op_sel_hi:[1,0]
	v_pk_mul_f32 v[112:113], v[112:113], s[22:23] op_sel_hi:[1,0]
	v_pk_mul_f32 v[114:115], v[114:115], s[22:23] op_sel_hi:[1,0]
	v_pk_mul_f32 v[116:117], v[116:117], s[22:23] op_sel_hi:[1,0]
	v_pk_mul_f32 v[118:119], v[118:119], s[22:23] op_sel_hi:[1,0]
	v_pk_mul_f32 v[120:121], v[120:121], s[22:23] op_sel_hi:[1,0]
	v_pk_mul_f32 v[122:123], v[122:123], s[22:23] op_sel_hi:[1,0]
	v_pk_mul_f32 v[124:125], v[124:125], s[22:23] op_sel_hi:[1,0]
	v_pk_mul_f32 v[126:127], v[126:127], s[22:23] op_sel_hi:[1,0]
	v_pk_mul_f32 v[128:129], v[128:129], s[22:23] op_sel_hi:[1,0]
	v_pk_mul_f32 v[130:131], v[130:131], s[22:23] op_sel_hi:[1,0]
	v_pk_mul_f32 v[132:133], v[132:133], s[22:23] op_sel_hi:[1,0]
	v_pk_mul_f32 v[134:135], v[134:135], s[22:23] op_sel_hi:[1,0]
	v_pk_mul_f32 v[136:137], v[136:137], s[22:23] op_sel_hi:[1,0]
	v_pk_mul_f32 v[138:139], v[138:139], s[22:23] op_sel_hi:[1,0]
	v_pk_mul_f32 v[140:141], v[140:141], s[22:23] op_sel_hi:[1,0]
	v_pk_mul_f32 v[142:143], v[142:143], s[22:23] op_sel_hi:[1,0]
	v_pk_mul_f32 v[144:145], v[144:145], s[22:23] op_sel_hi:[1,0]
	v_pk_mul_f32 v[146:147], v[146:147], s[22:23] op_sel_hi:[1,0]
	v_pk_mul_f32 v[148:149], v[148:149], s[22:23] op_sel_hi:[1,0]
	v_pk_mul_f32 v[150:151], v[150:151], s[22:23] op_sel_hi:[1,0]
	v_pk_mul_f32 v[152:153], v[152:153], s[22:23] op_sel_hi:[1,0]
	v_pk_mul_f32 v[154:155], v[154:155], s[22:23] op_sel_hi:[1,0]
	v_pk_mul_f32 v[156:157], v[156:157], s[22:23] op_sel_hi:[1,0]
	v_pk_mul_f32 v[158:159], v[158:159], s[22:23] op_sel_hi:[1,0]
	v_pk_mul_f32 v[160:161], v[160:161], s[22:23] op_sel_hi:[1,0]
	v_pk_mul_f32 v[162:163], v[162:163], s[22:23] op_sel_hi:[1,0]
	v_cvt_pk_fp8_f32 v74, v100, v104
	v_cvt_pk_fp8_f32 v75, v116, v120
	v_cvt_pk_fp8_f32 v76, v132, v136
	v_cvt_pk_fp8_f32 v77, v148, v152
	v_cvt_pk_fp8_f32 v74, v108, v112 op_sel:[0,0,1]
	v_cvt_pk_fp8_f32 v75, v124, v128 op_sel:[0,0,1]
	v_cvt_pk_fp8_f32 v76, v140, v144 op_sel:[0,0,1]
	v_cvt_pk_fp8_f32 v77, v156, v160 op_sel:[0,0,1]
	v_cvt_pk_fp8_f32 v84, v101, v105
	v_cvt_pk_fp8_f32 v85, v117, v121
	v_cvt_pk_fp8_f32 v86, v133, v137
	v_cvt_pk_fp8_f32 v87, v149, v153
	v_cvt_pk_fp8_f32 v84, v109, v113 op_sel:[0,0,1]
	v_cvt_pk_fp8_f32 v85, v125, v129 op_sel:[0,0,1]
	v_cvt_pk_fp8_f32 v86, v141, v145 op_sel:[0,0,1]
	v_cvt_pk_fp8_f32 v87, v157, v161 op_sel:[0,0,1]
	global_store_dwordx4 v6, v[74:77], s[26:27] nt
	v_cvt_pk_fp8_f32 v88, v102, v106
	v_cvt_pk_fp8_f32 v89, v118, v122
	v_cvt_pk_fp8_f32 v90, v134, v138
	v_cvt_pk_fp8_f32 v91, v150, v154
	v_cvt_pk_fp8_f32 v88, v110, v114 op_sel:[0,0,1]
	v_cvt_pk_fp8_f32 v89, v126, v130 op_sel:[0,0,1]
	v_cvt_pk_fp8_f32 v90, v142, v146 op_sel:[0,0,1]
	v_cvt_pk_fp8_f32 v91, v158, v162 op_sel:[0,0,1]
	global_store_dwordx4 v6, v[84:87], s[26:27] offset:2048 nt
	v_cvt_pk_fp8_f32 v92, v103, v107
	v_cvt_pk_fp8_f32 v93, v119, v123
	v_cvt_pk_fp8_f32 v94, v135, v139
	v_cvt_pk_fp8_f32 v95, v151, v155
	v_cvt_pk_fp8_f32 v92, v111, v115 op_sel:[0,0,1]
	v_cvt_pk_fp8_f32 v93, v127, v131 op_sel:[0,0,1]
	v_cvt_pk_fp8_f32 v94, v143, v147 op_sel:[0,0,1]
	v_cvt_pk_fp8_f32 v95, v159, v163 op_sel:[0,0,1]
	global_store_dwordx4 v9, v[88:91], s[26:27] nt
	s_nop 1
	global_store_dwordx4 v9, v[92:95], s[26:27] offset:2048 nt
	s_branch .Lcq_grab
.Lcq_done:
.LBB0_276:
	v_readlane_b32 s2, v254, 9
	v_readlane_b32 s3, v254, 10
	s_cmp_gt_i32 s3, 4
	s_cselect_b64 s[2:3], -1, 0
	s_and_b64 s[0:1], s[0:1], s[2:3]
	s_andn2_b64 vcc, exec, s[0:1]
	s_cbranch_vccnz .LBB0_330
	s_waitcnt vmcnt(0)
	s_waitcnt vmcnt(0)
	s_barrier
	s_mov_b64 s[0:1], exec
	v_readlane_b32 s4, v254, 14
	v_readlane_b32 s5, v254, 15
	s_and_b64 s[4:5], s[0:1], s[4:5]
	s_mov_b64 exec, s[4:5]
	s_cbranch_execz .LBB0_329
	s_add_i32 s4, 0, 0x20020
	v_mov_b32_e32 v1, s4
	s_waitcnt vmcnt(0) expcnt(0) lgkmcnt(0)
	ds_read_b32 v3, v1
	s_add_i32 s4, 0, 0x20024
	v_mov_b32_e32 v1, s4
	ds_read_b32 v1, v1
	s_waitcnt lgkmcnt(1)
	v_cmp_ne_u32_e32 vcc, 0, v3
	s_cbranch_vccnz .LBB0_293
	v_readlane_b32 s4, v254, 1
	v_readlane_b32 s5, v254, 2
	s_load_dwordx2 s[8:9], s[4:5], 0x4
	s_add_u32 s4, s88, 0x4200
	s_addc_u32 s5, s89, 0
	s_add_u32 s6, s88, 0x4400
	s_addc_u32 s7, s89, 0
	s_waitcnt lgkmcnt(0)
	s_mul_i32 s33, s8, s92
	s_add_u32 s8, s88, 0x4500
	s_mul_i32 s33, s33, s9
	s_addc_u32 s9, s89, 0
	s_add_u32 s10, s88, 0x4600
	s_addc_u32 s11, s89, 0
	s_add_u32 s12, s88, 0x4700
	s_addc_u32 s13, s89, 0
	s_add_u32 s14, s88, 0x4800
	s_addc_u32 s15, s89, 0
	s_add_u32 s16, s88, 0x4900
	s_addc_u32 s17, s89, 0
	s_add_u32 s18, s88, 0x4a00
	s_addc_u32 s19, s89, 0
	s_add_u32 s20, s88, 0x4b00
	s_addc_u32 s21, s89, 0
	s_add_u32 s22, s88, 0x4c00
	s_addc_u32 s23, s89, 0
	s_add_u32 s24, s88, 0x4d00
	s_addc_u32 s25, s89, 0
	s_add_u32 s26, s88, 0x4e00
	s_addc_u32 s27, s89, 0
	s_add_u32 s28, s88, 0x4f00
	s_addc_u32 s29, s89, 0
	s_add_u32 s30, s88, 0x5000
	s_addc_u32 s31, s89, 0
	s_add_u32 s34, s88, 0x5100
	s_addc_u32 s35, s89, 0
	s_add_u32 s36, s88, 0x5200
	s_addc_u32 s37, s89, 0
	s_add_u32 s38, s88, 0x5300
	s_addc_u32 s39, s89, 0
	s_mov_b32 s46, 1
	v_mov_b32_e32 v17, 0
	s_branch .LBB0_281
